# K1: each wave issues its eight 1KB loads in ascending address order
# speedup vs baseline: 1.0052x; 1.0052x over previous
.LBB0_6:
	s_lshr_b32 s12, s2, 3
	s_mov_b32 s13, 0
	s_and_b32 s3, s2, 7
	s_lshl_b64 s[0:1], s[12:13], 20
	v_lshrrev_b32_e32 v62, 6, v0
	v_and_b32_e32 v1, 63, v0
	v_lshlrev_b32_e32 v2, 13, v62
	v_lshlrev_b32_e32 v63, 4, v1
	v_lshl_add_u32 v2, s3, 17, v2
	v_or_b32_e32 v68, v2, v63
	s_mov_b32 s11, 0x20000
	s_mov_b32 s10, 0x100000
	s_waitcnt lgkmcnt(0)
	s_add_u32 s8, s4, s0
	s_addc_u32 s9, s5, s1
	s_and_b32 s9, s9, 0xffff
	v_mov_b32_e32 v46, v68
	buffer_load_dwordx4 v[26:29], v46, s[8:11], 0 offen sc0 nt
	buffer_load_dwordx4 v[10:13], v46, s[8:11], 0 offen offset:1024 sc0 nt
	buffer_load_dwordx4 v[34:37], v46, s[8:11], 0 offen offset:2048 sc0 nt
	buffer_load_dwordx4 v[14:17], v46, s[8:11], 0 offen offset:3072 sc0 nt
	v_add_u32_e32 v47, 0x1000, v46
	buffer_load_dwordx4 v[30:33], v47, s[8:11], 0 offen sc0 nt
	buffer_load_dwordx4 v[18:21], v47, s[8:11], 0 offen offset:1024 sc0 nt
	buffer_load_dwordx4 v[38:41], v47, s[8:11], 0 offen offset:2048 sc0 nt
	buffer_load_dwordx4 v[22:25], v47, s[8:11], 0 offen offset:3072 sc0 nt
	v_add_u32_e32 v46, 0x8000, v68
	buffer_load_dwordx4 v[96:99], v46, s[8:11], 0 offen sc0 nt
	buffer_load_dwordx4 v[80:83], v46, s[8:11], 0 offen offset:1024 sc0 nt
	buffer_load_dwordx4 v[104:107], v46, s[8:11], 0 offen offset:2048 sc0 nt
	buffer_load_dwordx4 v[84:87], v46, s[8:11], 0 offen offset:3072 sc0 nt
	v_add_u32_e32 v47, 0x1000, v46
	buffer_load_dwordx4 v[100:103], v47, s[8:11], 0 offen sc0 nt
	buffer_load_dwordx4 v[88:91], v47, s[8:11], 0 offen offset:1024 sc0 nt
	buffer_load_dwordx4 v[108:111], v47, s[8:11], 0 offen offset:2048 sc0 nt
	buffer_load_dwordx4 v[92:95], v47, s[8:11], 0 offen offset:3072 sc0 nt
	v_mbcnt_lo_u32_b32 v3, -1, 0
	v_mbcnt_hi_u32_b32 v3, -1, v3
	s_lshr_b32 s12, s2, 3
	s_mov_b32 s13, 0
	v_and_b32_e32 v5, 64, v3
	s_and_b32 s3, s2, 7
	s_lshl_b64 s[0:1], s[12:13], 20
	v_xor_b32_e32 v4, 16, v3
	v_add_u32_e32 v5, 64, v5
	s_waitcnt lgkmcnt(0)
	s_add_u32 s8, s4, s0
	v_cmp_lt_i32_e32 vcc, v4, v5
	v_lshrrev_b32_e32 v62, 6, v0
	s_addc_u32 s0, s5, s1
	s_lshl_b32 s12, s12, 9
	v_cndmask_b32_e32 v4, v3, v4, vcc
	s_and_b32 s9, s0, 0xffff
	v_lshlrev_b32_e32 v2, 2, v62
	v_lshlrev_b32_e32 v65, 2, v4
	v_xor_b32_e32 v4, 32, v3
	s_lshl_b64 s[4:5], s[12:13], 2
	v_and_b32_e32 v1, 63, v0
	v_cmp_lt_i32_e32 vcc, v4, v5
	v_lshl_add_u32 v66, s3, 6, v2
	s_add_u32 s4, s6, s4
	v_lshlrev_b32_e32 v2, 13, v62
	v_lshlrev_b32_e32 v63, 4, v1
	v_cndmask_b32_e32 v3, v3, v4, vcc
	v_lshlrev_b32_e32 v42, 2, v66
	v_mov_b32_e32 v43, 0
	s_addc_u32 s5, s7, s5
	v_lshl_add_u32 v2, s3, 17, v2
	s_mov_b32 s11, 0x20000
	s_mov_b32 s10, 0x100000
	v_lshlrev_b32_e32 v64, 2, v3
	v_cmp_eq_u32_e64 s[0:1], 0, v1
	v_lshl_add_u64 v[44:45], s[4:5], 0, v[42:43]
	v_lshrrev_b32_e32 v67, 2, v66
	v_or_b32_e32 v68, v2, v63
	v_mov_b32_e32 v42, v43
	v_mov_b32_e32 v2, v43
	v_mov_b32_e32 v3, v43
	v_mov_b32_e32 v4, v43
	v_mov_b32_e32 v5, v43
	v_mov_b32_e32 v6, v43
	v_mov_b32_e32 v7, v43
	v_mov_b32_e32 v8, v43
	v_mov_b32_e32 v9, v43
	s_sub_u32 s14, s2, 64
	s_cmp_lt_u32 s14, 6
	s_cbranch_scc0 .Lk1_nozero
	v_lshlrev_b32_e32 v69, 4, v0
	s_lshl_b32 s14, s14, 12
	v_add_u32_e32 v69, s14, v69
	v_add_u32_e32 v69, 0x582000, v69
	global_store_dwordx4 v69, v[2:5], s[6:7]

.LBB0_8:
	s_bitcmp1_b32 s15, 8
	s_cselect_b64 s[20:21], -1, 0
	s_lshr_b32 s16, s15, 2
	s_and_b32 s16, s16, 63
	s_lshl_b64 s[4:5], 1, s16
	s_waitcnt vmcnt(12)
	v_pk_add_f32 v[72:73], v[26:27], v[28:29]
	v_pk_add_f32 v[74:75], v[10:11], v[12:13]
	v_pk_add_f32 v[76:77], v[34:35], v[36:37]
	v_pk_add_f32 v[78:79], v[14:15], v[16:17]
	v_pk_add_f32 v[58:59], v[26:27], v[34:35]
	v_pk_add_f32 v[60:61], v[28:29], v[36:37]
	v_pk_add_f32 v[72:73], v[72:73], v[74:75]
	v_pk_add_f32 v[76:77], v[76:77], v[78:79]
	v_pk_add_f32 v[54:55], v[10:11], v[14:15]
	v_pk_add_f32 v[56:57], v[12:13], v[16:17]
	v_add_f32_e32 v50, v72, v73
	v_add_f32_e32 v51, v76, v77
	s_waitcnt vmcnt(8)
	v_pk_add_f32 v[72:73], v[30:31], v[32:33]
	v_pk_add_f32 v[74:75], v[18:19], v[20:21]
	v_pk_add_f32 v[76:77], v[38:39], v[40:41]
	v_pk_add_f32 v[78:79], v[22:23], v[24:25]
	v_pk_add_f32 v[48:49], v[30:31], v[38:39]
	v_pk_add_f32 v[70:71], v[32:33], v[40:41]
	v_pk_add_f32 v[72:73], v[72:73], v[74:75]
	v_pk_add_f32 v[76:77], v[76:77], v[78:79]
	v_pk_add_f32 v[58:59], v[58:59], v[48:49]
	v_pk_add_f32 v[60:61], v[60:61], v[70:71]
	v_pk_add_f32 v[48:49], v[18:19], v[22:23]
	v_pk_add_f32 v[70:71], v[20:21], v[24:25]
	v_add_f32_e32 v52, v72, v73
	v_add_f32_e32 v53, v76, v77
	v_pk_add_f32 v[2:3], v[2:3], v[58:59]
	v_pk_add_f32 v[4:5], v[4:5], v[60:61]
	v_pk_add_f32 v[54:55], v[54:55], v[48:49]
	v_pk_add_f32 v[56:57], v[56:57], v[70:71]
	v_add_f32_e32 v72, v50, v51
	v_add_f32_e32 v73, v52, v53
	v_pk_add_f32 v[6:7], v[6:7], v[54:55]
	v_pk_add_f32 v[8:9], v[8:9], v[56:57]
	v_add_f32_e32 v72, v72, v73
	v_add_f32_e32 v43, v43, v72
	v_add_f32_dpp v50, v50, v50 quad_perm:[1,0,3,2] row_mask:0xf bank_mask:0xf
	v_add_f32_dpp v51, v51, v51 quad_perm:[1,0,3,2] row_mask:0xf bank_mask:0xf
	v_add_f32_dpp v52, v52, v52 quad_perm:[1,0,3,2] row_mask:0xf bank_mask:0xf
	v_add_f32_dpp v53, v53, v53 quad_perm:[1,0,3,2] row_mask:0xf bank_mask:0xf
	v_add_f32_dpp v50, v50, v50 quad_perm:[2,3,0,1] row_mask:0xf bank_mask:0xf
	v_add_f32_dpp v51, v51, v51 quad_perm:[2,3,0,1] row_mask:0xf bank_mask:0xf
	v_add_f32_dpp v52, v52, v52 quad_perm:[2,3,0,1] row_mask:0xf bank_mask:0xf
	v_add_f32_dpp v53, v53, v53 quad_perm:[2,3,0,1] row_mask:0xf bank_mask:0xf
	v_add_f32_dpp v50, v50, v50 row_half_mirror row_mask:0xf bank_mask:0xf
	v_add_f32_dpp v51, v51, v51 row_half_mirror row_mask:0xf bank_mask:0xf
	v_add_f32_dpp v52, v52, v52 row_half_mirror row_mask:0xf bank_mask:0xf
	v_add_f32_dpp v53, v53, v53 row_half_mirror row_mask:0xf bank_mask:0xf
	v_add_f32_dpp v50, v50, v50 row_mirror row_mask:0xf bank_mask:0xf
	v_add_f32_dpp v51, v51, v51 row_mirror row_mask:0xf bank_mask:0xf
	v_add_f32_dpp v52, v52, v52 row_mirror row_mask:0xf bank_mask:0xf
	v_add_f32_dpp v53, v53, v53 row_mirror row_mask:0xf bank_mask:0xf
	v_add_f32_dpp v50, v50, v50 row_bcast:15 row_mask:0xa bank_mask:0xf
	v_add_f32_dpp v51, v51, v51 row_bcast:15 row_mask:0xa bank_mask:0xf
	v_add_f32_dpp v52, v52, v52 row_bcast:15 row_mask:0xa bank_mask:0xf
	v_add_f32_dpp v53, v53, v53 row_bcast:15 row_mask:0xa bank_mask:0xf
	v_add_f32_dpp v50, v50, v50 row_bcast:31 row_mask:0xc bank_mask:0xf
	v_add_f32_dpp v51, v51, v51 row_bcast:31 row_mask:0xc bank_mask:0xf
	v_add_f32_dpp v52, v52, v52 row_bcast:31 row_mask:0xc bank_mask:0xf
	v_add_f32_dpp v53, v53, v53 row_bcast:31 row_mask:0xc bank_mask:0xf
	s_mov_b64 exec, s[4:5]
	v_cndmask_b32_e64 v58, v26, v10, s[20:21]
	v_cndmask_b32_e64 v59, v35, v15, s[20:21]
	v_cndmask_b32_e64 v60, v32, v20, s[20:21]
	v_cndmask_b32_e64 v61, v41, v25, s[20:21]
	global_store_dwordx4 v[44:45], v[58:61], off
	v_add_f32_e32 v72, v58, v59
	v_add_f32_e32 v73, v60, v61
	v_add_f32_e32 v72, v72, v73
	v_add_f32_e32 v42, v42, v72
	s_mov_b32 s4, 0
	s_brev_b32 s5, 1
	s_mov_b64 exec, s[4:5]
	v_lshl_add_u64 v[72:73], v[44:45], 0, s[18:19]
	global_store_dwordx4 v[72:73], v[50:53], off
	s_mov_b64 exec, -1
	s_add_u32 s15, s15, 16
	v_lshl_add_u64 v[44:45], v[44:45], 0, 64
	v_add_u32_e32 v46, 0x10000, v68
	buffer_load_dwordx4 v[26:29], v46, s[8:11], 0 offen sc0 nt
	buffer_load_dwordx4 v[10:13], v46, s[8:11], 0 offen offset:1024 sc0 nt
	buffer_load_dwordx4 v[34:37], v46, s[8:11], 0 offen offset:2048 sc0 nt
	buffer_load_dwordx4 v[14:17], v46, s[8:11], 0 offen offset:3072 sc0 nt
	v_add_u32_e32 v47, 0x1000, v46
	buffer_load_dwordx4 v[30:33], v47, s[8:11], 0 offen sc0 nt
	buffer_load_dwordx4 v[18:21], v47, s[8:11], 0 offen offset:1024 sc0 nt
	buffer_load_dwordx4 v[38:41], v47, s[8:11], 0 offen offset:2048 sc0 nt
	buffer_load_dwordx4 v[22:25], v47, s[8:11], 0 offen offset:3072 sc0 nt
	s_bitcmp1_b32 s15, 8
	s_cselect_b64 s[20:21], -1, 0
	s_lshr_b32 s16, s15, 2
	s_and_b32 s16, s16, 63
	s_lshl_b64 s[4:5], 1, s16
	s_waitcnt vmcnt(14)
	v_pk_add_f32 v[72:73], v[96:97], v[98:99]
	v_pk_add_f32 v[74:75], v[80:81], v[82:83]
	v_pk_add_f32 v[76:77], v[104:105], v[106:107]
	v_pk_add_f32 v[78:79], v[84:85], v[86:87]
	v_pk_add_f32 v[58:59], v[96:97], v[104:105]
	v_pk_add_f32 v[60:61], v[98:99], v[106:107]
	v_pk_add_f32 v[72:73], v[72:73], v[74:75]
	v_pk_add_f32 v[76:77], v[76:77], v[78:79]
	v_pk_add_f32 v[54:55], v[80:81], v[84:85]
	v_pk_add_f32 v[56:57], v[82:83], v[86:87]
	v_add_f32_e32 v50, v72, v73
	v_add_f32_e32 v51, v76, v77
	s_waitcnt vmcnt(10)
	v_pk_add_f32 v[72:73], v[100:101], v[102:103]
	v_pk_add_f32 v[74:75], v[88:89], v[90:91]
	v_pk_add_f32 v[76:77], v[108:109], v[110:111]
	v_pk_add_f32 v[78:79], v[92:93], v[94:95]
	v_pk_add_f32 v[48:49], v[100:101], v[108:109]
	v_pk_add_f32 v[70:71], v[102:103], v[110:111]
	v_pk_add_f32 v[72:73], v[72:73], v[74:75]
	v_pk_add_f32 v[76:77], v[76:77], v[78:79]
	v_pk_add_f32 v[58:59], v[58:59], v[48:49]
	v_pk_add_f32 v[60:61], v[60:61], v[70:71]
	v_pk_add_f32 v[48:49], v[88:89], v[92:93]
	v_pk_add_f32 v[70:71], v[90:91], v[94:95]
	v_add_f32_e32 v52, v72, v73
	v_add_f32_e32 v53, v76, v77
	v_pk_add_f32 v[2:3], v[2:3], v[58:59]
	v_pk_add_f32 v[4:5], v[4:5], v[60:61]
	v_pk_add_f32 v[54:55], v[54:55], v[48:49]
	v_pk_add_f32 v[56:57], v[56:57], v[70:71]
	v_add_f32_e32 v72, v50, v51
	v_add_f32_e32 v73, v52, v53
	v_pk_add_f32 v[6:7], v[6:7], v[54:55]
	v_pk_add_f32 v[8:9], v[8:9], v[56:57]
	v_add_f32_e32 v72, v72, v73
	v_add_f32_e32 v43, v43, v72
	v_add_f32_dpp v50, v50, v50 quad_perm:[1,0,3,2] row_mask:0xf bank_mask:0xf
	v_add_f32_dpp v51, v51, v51 quad_perm:[1,0,3,2] row_mask:0xf bank_mask:0xf
	v_add_f32_dpp v52, v52, v52 quad_perm:[1,0,3,2] row_mask:0xf bank_mask:0xf
	v_add_f32_dpp v53, v53, v53 quad_perm:[1,0,3,2] row_mask:0xf bank_mask:0xf
	v_add_f32_dpp v50, v50, v50 quad_perm:[2,3,0,1] row_mask:0xf bank_mask:0xf
	v_add_f32_dpp v51, v51, v51 quad_perm:[2,3,0,1] row_mask:0xf bank_mask:0xf
	v_add_f32_dpp v52, v52, v52 quad_perm:[2,3,0,1] row_mask:0xf bank_mask:0xf
	v_add_f32_dpp v53, v53, v53 quad_perm:[2,3,0,1] row_mask:0xf bank_mask:0xf
	v_add_f32_dpp v50, v50, v50 row_half_mirror row_mask:0xf bank_mask:0xf
	v_add_f32_dpp v51, v51, v51 row_half_mirror row_mask:0xf bank_mask:0xf
	v_add_f32_dpp v52, v52, v52 row_half_mirror row_mask:0xf bank_mask:0xf
	v_add_f32_dpp v53, v53, v53 row_half_mirror row_mask:0xf bank_mask:0xf
	v_add_f32_dpp v50, v50, v50 row_mirror row_mask:0xf bank_mask:0xf
	v_add_f32_dpp v51, v51, v51 row_mirror row_mask:0xf bank_mask:0xf
	v_add_f32_dpp v52, v52, v52 row_mirror row_mask:0xf bank_mask:0xf
	v_add_f32_dpp v53, v53, v53 row_mirror row_mask:0xf bank_mask:0xf
	v_add_f32_dpp v50, v50, v50 row_bcast:15 row_mask:0xa bank_mask:0xf
	v_add_f32_dpp v51, v51, v51 row_bcast:15 row_mask:0xa bank_mask:0xf
	v_add_f32_dpp v52, v52, v52 row_bcast:15 row_mask:0xa bank_mask:0xf
	v_add_f32_dpp v53, v53, v53 row_bcast:15 row_mask:0xa bank_mask:0xf
	v_add_f32_dpp v50, v50, v50 row_bcast:31 row_mask:0xc bank_mask:0xf
	v_add_f32_dpp v51, v51, v51 row_bcast:31 row_mask:0xc bank_mask:0xf
	v_add_f32_dpp v52, v52, v52 row_bcast:31 row_mask:0xc bank_mask:0xf
	v_add_f32_dpp v53, v53, v53 row_bcast:31 row_mask:0xc bank_mask:0xf
	s_mov_b64 exec, s[4:5]
	v_cndmask_b32_e64 v58, v96, v80, s[20:21]
	v_cndmask_b32_e64 v59, v105, v85, s[20:21]
	v_cndmask_b32_e64 v60, v102, v90, s[20:21]
	v_cndmask_b32_e64 v61, v111, v95, s[20:21]
	global_store_dwordx4 v[44:45], v[58:61], off
	v_add_f32_e32 v72, v58, v59
	v_add_f32_e32 v73, v60, v61
	v_add_f32_e32 v72, v72, v73
	v_add_f32_e32 v42, v42, v72
	s_mov_b32 s4, 0
	s_brev_b32 s5, 1
	s_mov_b64 exec, s[4:5]
	v_lshl_add_u64 v[72:73], v[44:45], 0, s[18:19]
	global_store_dwordx4 v[72:73], v[50:53], off
	s_mov_b64 exec, -1
	s_add_u32 s15, s15, 16
	v_lshl_add_u64 v[44:45], v[44:45], 0, 64
	v_add_u32_e32 v46, 0x18000, v68
	buffer_load_dwordx4 v[96:99], v46, s[8:11], 0 offen sc0 nt
	buffer_load_dwordx4 v[80:83], v46, s[8:11], 0 offen offset:1024 sc0 nt
	buffer_load_dwordx4 v[104:107], v46, s[8:11], 0 offen offset:2048 sc0 nt
	buffer_load_dwordx4 v[84:87], v46, s[8:11], 0 offen offset:3072 sc0 nt
	v_add_u32_e32 v47, 0x1000, v46
	buffer_load_dwordx4 v[100:103], v47, s[8:11], 0 offen sc0 nt
	buffer_load_dwordx4 v[88:91], v47, s[8:11], 0 offen offset:1024 sc0 nt
	buffer_load_dwordx4 v[108:111], v47, s[8:11], 0 offen offset:2048 sc0 nt
	buffer_load_dwordx4 v[92:95], v47, s[8:11], 0 offen offset:3072 sc0 nt
	s_bitcmp1_b32 s15, 8
	s_cselect_b64 s[20:21], -1, 0
	s_lshr_b32 s16, s15, 2
	s_and_b32 s16, s16, 63
	s_lshl_b64 s[4:5], 1, s16
	s_waitcnt vmcnt(14)
	v_pk_add_f32 v[72:73], v[26:27], v[28:29]
	v_pk_add_f32 v[74:75], v[10:11], v[12:13]
	v_pk_add_f32 v[76:77], v[34:35], v[36:37]
	v_pk_add_f32 v[78:79], v[14:15], v[16:17]
	v_pk_add_f32 v[58:59], v[26:27], v[34:35]
	v_pk_add_f32 v[60:61], v[28:29], v[36:37]
	v_pk_add_f32 v[72:73], v[72:73], v[74:75]
	v_pk_add_f32 v[76:77], v[76:77], v[78:79]
	v_pk_add_f32 v[54:55], v[10:11], v[14:15]
	v_pk_add_f32 v[56:57], v[12:13], v[16:17]
	v_add_f32_e32 v50, v72, v73
	v_add_f32_e32 v51, v76, v77
	s_waitcnt vmcnt(10)
	v_pk_add_f32 v[72:73], v[30:31], v[32:33]
	v_pk_add_f32 v[74:75], v[18:19], v[20:21]
	v_pk_add_f32 v[76:77], v[38:39], v[40:41]
	v_pk_add_f32 v[78:79], v[22:23], v[24:25]
	v_pk_add_f32 v[48:49], v[30:31], v[38:39]
	v_pk_add_f32 v[70:71], v[32:33], v[40:41]
	v_pk_add_f32 v[72:73], v[72:73], v[74:75]
	v_pk_add_f32 v[76:77], v[76:77], v[78:79]
	v_pk_add_f32 v[58:59], v[58:59], v[48:49]
	v_pk_add_f32 v[60:61], v[60:61], v[70:71]
	v_pk_add_f32 v[48:49], v[18:19], v[22:23]
	v_pk_add_f32 v[70:71], v[20:21], v[24:25]
	v_add_f32_e32 v52, v72, v73
	v_add_f32_e32 v53, v76, v77
	v_pk_add_f32 v[2:3], v[2:3], v[58:59]
	v_pk_add_f32 v[4:5], v[4:5], v[60:61]
	v_pk_add_f32 v[54:55], v[54:55], v[48:49]
	v_pk_add_f32 v[56:57], v[56:57], v[70:71]
	v_add_f32_e32 v72, v50, v51
	v_add_f32_e32 v73, v52, v53
	v_pk_add_f32 v[6:7], v[6:7], v[54:55]
	v_pk_add_f32 v[8:9], v[8:9], v[56:57]
	v_add_f32_e32 v72, v72, v73
	v_add_f32_e32 v43, v43, v72
	v_add_f32_dpp v50, v50, v50 quad_perm:[1,0,3,2] row_mask:0xf bank_mask:0xf
	v_add_f32_dpp v51, v51, v51 quad_perm:[1,0,3,2] row_mask:0xf bank_mask:0xf
	v_add_f32_dpp v52, v52, v52 quad_perm:[1,0,3,2] row_mask:0xf bank_mask:0xf
	v_add_f32_dpp v53, v53, v53 quad_perm:[1,0,3,2] row_mask:0xf bank_mask:0xf
	v_add_f32_dpp v50, v50, v50 quad_perm:[2,3,0,1] row_mask:0xf bank_mask:0xf
	v_add_f32_dpp v51, v51, v51 quad_perm:[2,3,0,1] row_mask:0xf bank_mask:0xf
	v_add_f32_dpp v52, v52, v52 quad_perm:[2,3,0,1] row_mask:0xf bank_mask:0xf
	v_add_f32_dpp v53, v53, v53 quad_perm:[2,3,0,1] row_mask:0xf bank_mask:0xf
	v_add_f32_dpp v50, v50, v50 row_half_mirror row_mask:0xf bank_mask:0xf
	v_add_f32_dpp v51, v51, v51 row_half_mirror row_mask:0xf bank_mask:0xf
	v_add_f32_dpp v52, v52, v52 row_half_mirror row_mask:0xf bank_mask:0xf
	v_add_f32_dpp v53, v53, v53 row_half_mirror row_mask:0xf bank_mask:0xf
	v_add_f32_dpp v50, v50, v50 row_mirror row_mask:0xf bank_mask:0xf
	v_add_f32_dpp v51, v51, v51 row_mirror row_mask:0xf bank_mask:0xf
	v_add_f32_dpp v52, v52, v52 row_mirror row_mask:0xf bank_mask:0xf
	v_add_f32_dpp v53, v53, v53 row_mirror row_mask:0xf bank_mask:0xf
	v_add_f32_dpp v50, v50, v50 row_bcast:15 row_mask:0xa bank_mask:0xf
	v_add_f32_dpp v51, v51, v51 row_bcast:15 row_mask:0xa bank_mask:0xf
	v_add_f32_dpp v52, v52, v52 row_bcast:15 row_mask:0xa bank_mask:0xf
	v_add_f32_dpp v53, v53, v53 row_bcast:15 row_mask:0xa bank_mask:0xf
	v_add_f32_dpp v50, v50, v50 row_bcast:31 row_mask:0xc bank_mask:0xf
	v_add_f32_dpp v51, v51, v51 row_bcast:31 row_mask:0xc bank_mask:0xf
	v_add_f32_dpp v52, v52, v52 row_bcast:31 row_mask:0xc bank_mask:0xf
	v_add_f32_dpp v53, v53, v53 row_bcast:31 row_mask:0xc bank_mask:0xf
	s_mov_b64 exec, s[4:5]
	v_cndmask_b32_e64 v58, v26, v10, s[20:21]
	v_cndmask_b32_e64 v59, v35, v15, s[20:21]
	v_cndmask_b32_e64 v60, v32, v20, s[20:21]
	v_cndmask_b32_e64 v61, v41, v25, s[20:21]
	global_store_dwordx4 v[44:45], v[58:61], off
	v_add_f32_e32 v72, v58, v59
	v_add_f32_e32 v73, v60, v61
	v_add_f32_e32 v72, v72, v73
	v_add_f32_e32 v42, v42, v72
	s_mov_b32 s4, 0
	s_brev_b32 s5, 1
	s_mov_b64 exec, s[4:5]
	v_lshl_add_u64 v[72:73], v[44:45], 0, s[18:19]
	global_store_dwordx4 v[72:73], v[50:53], off
	s_mov_b64 exec, -1
	s_add_u32 s15, s15, 16
	v_lshl_add_u64 v[44:45], v[44:45], 0, 64
	s_bitcmp1_b32 s15, 8
	s_cselect_b64 s[20:21], -1, 0
	s_lshr_b32 s16, s15, 2
	s_and_b32 s16, s16, 63
	s_lshl_b64 s[4:5], 1, s16
	s_waitcnt vmcnt(6)
	v_pk_add_f32 v[72:73], v[96:97], v[98:99]
	v_pk_add_f32 v[74:75], v[80:81], v[82:83]
	v_pk_add_f32 v[76:77], v[104:105], v[106:107]
	v_pk_add_f32 v[78:79], v[84:85], v[86:87]
	v_pk_add_f32 v[58:59], v[96:97], v[104:105]
	v_pk_add_f32 v[60:61], v[98:99], v[106:107]
	v_pk_add_f32 v[72:73], v[72:73], v[74:75]
	v_pk_add_f32 v[76:77], v[76:77], v[78:79]
	v_pk_add_f32 v[54:55], v[80:81], v[84:85]
	v_pk_add_f32 v[56:57], v[82:83], v[86:87]
	v_add_f32_e32 v50, v72, v73
	v_add_f32_e32 v51, v76, v77
	s_waitcnt vmcnt(2)
	v_pk_add_f32 v[72:73], v[100:101], v[102:103]
	v_pk_add_f32 v[74:75], v[88:89], v[90:91]
	v_pk_add_f32 v[76:77], v[108:109], v[110:111]
	v_pk_add_f32 v[78:79], v[92:93], v[94:95]
	v_pk_add_f32 v[48:49], v[100:101], v[108:109]
	v_pk_add_f32 v[70:71], v[102:103], v[110:111]
	v_pk_add_f32 v[72:73], v[72:73], v[74:75]
	v_pk_add_f32 v[76:77], v[76:77], v[78:79]
	v_pk_add_f32 v[58:59], v[58:59], v[48:49]
	v_pk_add_f32 v[60:61], v[60:61], v[70:71]
	v_pk_add_f32 v[48:49], v[88:89], v[92:93]
	v_pk_add_f32 v[70:71], v[90:91], v[94:95]
	v_add_f32_e32 v52, v72, v73
	v_add_f32_e32 v53, v76, v77
	v_pk_add_f32 v[2:3], v[2:3], v[58:59]
	v_pk_add_f32 v[4:5], v[4:5], v[60:61]
	v_pk_add_f32 v[54:55], v[54:55], v[48:49]
	v_pk_add_f32 v[56:57], v[56:57], v[70:71]
	v_add_f32_e32 v72, v50, v51
	v_add_f32_e32 v73, v52, v53
	v_pk_add_f32 v[6:7], v[6:7], v[54:55]
	v_pk_add_f32 v[8:9], v[8:9], v[56:57]
	v_add_f32_e32 v72, v72, v73
	v_add_f32_e32 v43, v43, v72
	v_add_f32_dpp v50, v50, v50 quad_perm:[1,0,3,2] row_mask:0xf bank_mask:0xf
	v_add_f32_dpp v51, v51, v51 quad_perm:[1,0,3,2] row_mask:0xf bank_mask:0xf
	v_add_f32_dpp v52, v52, v52 quad_perm:[1,0,3,2] row_mask:0xf bank_mask:0xf
	v_add_f32_dpp v53, v53, v53 quad_perm:[1,0,3,2] row_mask:0xf bank_mask:0xf
	v_add_f32_dpp v50, v50, v50 quad_perm:[2,3,0,1] row_mask:0xf bank_mask:0xf
	v_add_f32_dpp v51, v51, v51 quad_perm:[2,3,0,1] row_mask:0xf bank_mask:0xf
	v_add_f32_dpp v52, v52, v52 quad_perm:[2,3,0,1] row_mask:0xf bank_mask:0xf
	v_add_f32_dpp v53, v53, v53 quad_perm:[2,3,0,1] row_mask:0xf bank_mask:0xf
	v_add_f32_dpp v50, v50, v50 row_half_mirror row_mask:0xf bank_mask:0xf
	v_add_f32_dpp v51, v51, v51 row_half_mirror row_mask:0xf bank_mask:0xf
	v_add_f32_dpp v52, v52, v52 row_half_mirror row_mask:0xf bank_mask:0xf
	v_add_f32_dpp v53, v53, v53 row_half_mirror row_mask:0xf bank_mask:0xf
	v_add_f32_dpp v50, v50, v50 row_mirror row_mask:0xf bank_mask:0xf
	v_add_f32_dpp v51, v51, v51 row_mirror row_mask:0xf bank_mask:0xf
	v_add_f32_dpp v52, v52, v52 row_mirror row_mask:0xf bank_mask:0xf
	v_add_f32_dpp v53, v53, v53 row_mirror row_mask:0xf bank_mask:0xf
	v_add_f32_dpp v50, v50, v50 row_bcast:15 row_mask:0xa bank_mask:0xf
	v_add_f32_dpp v51, v51, v51 row_bcast:15 row_mask:0xa bank_mask:0xf
	v_add_f32_dpp v52, v52, v52 row_bcast:15 row_mask:0xa bank_mask:0xf
	v_add_f32_dpp v53, v53, v53 row_bcast:15 row_mask:0xa bank_mask:0xf
	v_add_f32_dpp v50, v50, v50 row_bcast:31 row_mask:0xc bank_mask:0xf
	v_add_f32_dpp v51, v51, v51 row_bcast:31 row_mask:0xc bank_mask:0xf
	v_add_f32_dpp v52, v52, v52 row_bcast:31 row_mask:0xc bank_mask:0xf
	v_add_f32_dpp v53, v53, v53 row_bcast:31 row_mask:0xc bank_mask:0xf
	s_mov_b64 exec, s[4:5]
	v_cndmask_b32_e64 v58, v96, v80, s[20:21]
	v_cndmask_b32_e64 v59, v105, v85, s[20:21]
	v_cndmask_b32_e64 v60, v102, v90, s[20:21]
	v_cndmask_b32_e64 v61, v111, v95, s[20:21]
	global_store_dwordx4 v[44:45], v[58:61], off
	v_add_f32_e32 v72, v58, v59
	v_add_f32_e32 v73, v60, v61
	v_add_f32_e32 v72, v72, v73
	v_add_f32_e32 v42, v42, v72
	s_mov_b32 s4, 0
	s_brev_b32 s5, 1
	s_mov_b64 exec, s[4:5]
	v_lshl_add_u64 v[72:73], v[44:45], 0, s[18:19]
	global_store_dwordx4 v[72:73], v[50:53], off
	s_mov_b64 exec, -1
	s_add_u32 s15, s15, 16
	v_lshl_add_u64 v[44:45], v[44:45], 0, 64
